# v13_nop8
# baseline (speedup 1.0000x reference)
.Lp1_go_1:
	v_accvgpr_write_b32 a4, v137
	v_accvgpr_write_b32 a5, v138
	v_accvgpr_write_b32 a6, v139
	v_readlane_b32 s54, v66, 0
	v_accvgpr_write_b32 a7, v140
	v_cmp_lt_i32_e32 vcc, 0, v136
	v_rcp_f32_e64 v73, -s54
	v_writelane_b32 v166, s54, 0
	v_cndmask_b32_e64 v72, 0, v66, s[6:7]
	v_mul_f32_e32 v70, v72, v73
	s_nop 1
	v_mfma_f32_16x16x4_f32 v[66:69], v70, v66, v[66:69]
	v_mfma_f32_16x16x4_f32 a[4:7], v70, v137, a[4:7]
	s_nop 8
	v_readlane_b32 s54, v67, 1
	v_cndmask_b32_e64 v72, 0, v67, s[8:9]
	s_nop 0
	v_rcp_f32_e64 v73, -s54
	v_writelane_b32 v166, s54, 1
	v_mul_f32_e32 v71, v72, v73
	s_nop 1
	v_mfma_f32_16x16x4_f32 v[66:69], v71, v67, v[66:69]
	v_mfma_f32_16x16x4_f32 a[4:7], v71, a5, a[4:7]
	s_nop 8
	v_readlane_b32 s54, v68, 2
	v_cndmask_b32_e64 v72, 0, v68, s[10:11]
	s_nop 0
	v_rcp_f32_e64 v73, -s54
	v_writelane_b32 v166, s54, 2
	v_mul_f32_e32 v70, v72, v73
	s_nop 1
	v_mfma_f32_16x16x4_f32 v[66:69], v70, v68, v[66:69]
	v_mfma_f32_16x16x4_f32 a[4:7], v70, a6, a[4:7]
	s_nop 8
	v_readlane_b32 s54, v69, 3
	v_cndmask_b32_e64 v72, 0, v69, s[12:13]
	s_nop 0
	v_rcp_f32_e64 v73, -s54
	v_writelane_b32 v166, s54, 3
	v_mul_f32_e32 v71, v72, v73
	s_nop 1
	v_mfma_f32_16x16x4_f32 v[66:69], v71, v69, v[66:69]
	v_mfma_f32_16x16x4_f32 a[4:7], v71, a7, a[4:7]
	s_nop 8
	v_readlane_b32 s54, v66, 20
	v_cndmask_b32_e64 v72, 0, v66, s[14:15]
	s_nop 0
	v_rcp_f32_e64 v73, -s54
	v_writelane_b32 v166, s54, 4
	v_mul_f32_e32 v70, v72, v73
	s_nop 1
	v_mfma_f32_16x16x4_f32 v[66:69], v70, v66, v[66:69]
	v_mfma_f32_16x16x4_f32 a[4:7], v70, a4, a[4:7]
	s_nop 8
	v_readlane_b32 s54, v67, 21
	v_cndmask_b32_e64 v72, 0, v67, s[16:17]
	s_nop 0
	v_rcp_f32_e64 v73, -s54
	v_writelane_b32 v166, s54, 5
	v_mul_f32_e32 v71, v72, v73
	s_nop 1
	v_mfma_f32_16x16x4_f32 v[66:69], v71, v67, v[66:69]
	v_mfma_f32_16x16x4_f32 a[4:7], v71, a5, a[4:7]
	s_nop 8
	v_readlane_b32 s54, v68, 22
	v_cndmask_b32_e64 v72, 0, v68, s[18:19]
	s_nop 0
	v_rcp_f32_e64 v73, -s54
	v_writelane_b32 v166, s54, 6
	v_mul_f32_e32 v70, v72, v73
	s_nop 1
	v_mfma_f32_16x16x4_f32 v[66:69], v70, v68, v[66:69]
	v_mfma_f32_16x16x4_f32 a[4:7], v70, a6, a[4:7]
	s_nop 8
	v_readlane_b32 s54, v69, 23
	v_cndmask_b32_e64 v72, 0, v69, s[20:21]
	s_nop 0
	v_rcp_f32_e64 v73, -s54
	v_writelane_b32 v166, s54, 7
	v_mul_f32_e32 v71, v72, v73
	s_nop 1
	v_mfma_f32_16x16x4_f32 v[66:69], v71, v69, v[66:69]
	v_mfma_f32_16x16x4_f32 a[4:7], v71, a7, a[4:7]
	s_nop 8
	v_readlane_b32 s54, v66, 40
	v_cndmask_b32_e64 v72, 0, v66, s[22:23]
	s_nop 0
	v_rcp_f32_e64 v73, -s54
	v_writelane_b32 v166, s54, 8
	v_mul_f32_e32 v70, v72, v73
	s_nop 1
	v_mfma_f32_16x16x4_f32 v[66:69], v70, v66, v[66:69]
	v_mfma_f32_16x16x4_f32 a[4:7], v70, a4, a[4:7]
	s_nop 8
	v_readlane_b32 s54, v67, 41
	v_cndmask_b32_e64 v72, 0, v67, s[24:25]
	s_nop 0
	v_rcp_f32_e64 v73, -s54
	v_writelane_b32 v166, s54, 9
	v_mul_f32_e32 v71, v72, v73
	s_nop 1
	v_mfma_f32_16x16x4_f32 v[66:69], v71, v67, v[66:69]
	v_mfma_f32_16x16x4_f32 a[4:7], v71, a5, a[4:7]
	s_nop 8
	v_readlane_b32 s54, v68, 42
	v_cndmask_b32_e64 v72, 0, v68, s[26:27]
	s_nop 0
	v_rcp_f32_e64 v73, -s54
	v_writelane_b32 v166, s54, 10
	v_mul_f32_e32 v70, v72, v73
	s_nop 1
	v_mfma_f32_16x16x4_f32 v[66:69], v70, v68, v[66:69]
	v_mfma_f32_16x16x4_f32 a[4:7], v70, a6, a[4:7]
	s_nop 8
	v_readlane_b32 s54, v69, 43
	v_cndmask_b32_e64 v72, 0, v69, s[28:29]
	s_nop 0
	v_rcp_f32_e64 v73, -s54
	v_writelane_b32 v166, s54, 11
	v_mul_f32_e32 v71, v72, v73
	s_nop 1
	v_mfma_f32_16x16x4_f32 v[66:69], v71, v69, v[66:69]
	v_mfma_f32_16x16x4_f32 a[4:7], v71, a7, a[4:7]
	s_nop 8
	v_readlane_b32 s54, v66, 60
	v_cndmask_b32_e64 v72, 0, v66, s[30:31]
	s_nop 0
	v_rcp_f32_e64 v73, -s54
	v_writelane_b32 v166, s54, 12
	v_mul_f32_e32 v70, v72, v73
	s_nop 1
	v_mfma_f32_16x16x4_f32 v[66:69], v70, v66, v[66:69]
	v_mfma_f32_16x16x4_f32 a[4:7], v70, a4, a[4:7]
	s_nop 8
	v_readlane_b32 s54, v67, 61
	v_cndmask_b32_e64 v72, 0, v67, s[34:35]
	s_nop 0
	v_rcp_f32_e64 v73, -s54
	v_writelane_b32 v166, s54, 13
	v_mul_f32_e32 v71, v72, v73
	s_nop 1
	v_mfma_f32_16x16x4_f32 v[66:69], v71, v67, v[66:69]
	v_mfma_f32_16x16x4_f32 a[4:7], v71, a5, a[4:7]
	s_nop 8
	v_readlane_b32 s54, v68, 62
	v_cndmask_b32_e64 v72, 0, v68, s[36:37]
	s_nop 0
	v_rcp_f32_e64 v73, -s54
	v_writelane_b32 v166, s54, 14
	v_mul_f32_e32 v70, v72, v73
	s_nop 1
	v_mfma_f32_16x16x4_f32 v[66:69], v70, v68, v[66:69]
	v_mfma_f32_16x16x4_f32 a[4:7], v70, a6, a[4:7]
	s_nop 8
	v_readlane_b32 s54, v69, 63
	s_nop 1
	v_writelane_b32 v166, s54, 15
	v_accvgpr_read_b32 v73, a7
	v_accvgpr_read_b32 v72, a6
	v_accvgpr_read_b32 v71, a5
	v_accvgpr_read_b32 v70, a4
	s_and_saveexec_b64 s[54:55], s[4:5]
	s_cbranch_execz .LBB1_113
	s_waitcnt lgkmcnt(2)
	v_lshl_add_u32 v167, s96, 2, v134
	ds_write_b32 v167, v166

.Lp1_go_2:
	v_accvgpr_write_b32 a4, v137
	v_accvgpr_write_b32 a5, v138
	v_accvgpr_write_b32 a6, v139
	v_readlane_b32 s52, v2, 0
	v_accvgpr_write_b32 a7, v140
	v_cmp_lt_i32_e32 vcc, 0, v136
	v_rcp_f32_e64 v9, -s52
	v_writelane_b32 v16, s52, 0
	v_cndmask_b32_e64 v8, 0, v2, s[6:7]
	v_mul_f32_e32 v6, v8, v9
	s_nop 1
	v_mfma_f32_16x16x4_f32 v[2:5], v6, v2, v[2:5]
	v_mfma_f32_16x16x4_f32 a[4:7], v6, v137, a[4:7]
	s_nop 8
	v_readlane_b32 s52, v3, 1
	v_cndmask_b32_e64 v8, 0, v3, s[8:9]
	s_nop 0
	v_rcp_f32_e64 v9, -s52
	v_writelane_b32 v16, s52, 1
	v_mul_f32_e32 v7, v8, v9
	s_nop 1
	v_mfma_f32_16x16x4_f32 v[2:5], v7, v3, v[2:5]
	v_mfma_f32_16x16x4_f32 a[4:7], v7, a5, a[4:7]
	s_nop 8
	v_readlane_b32 s52, v4, 2
	v_cndmask_b32_e64 v8, 0, v4, s[10:11]
	s_nop 0
	v_rcp_f32_e64 v9, -s52
	v_writelane_b32 v16, s52, 2
	v_mul_f32_e32 v6, v8, v9
	s_nop 1
	v_mfma_f32_16x16x4_f32 v[2:5], v6, v4, v[2:5]
	v_mfma_f32_16x16x4_f32 a[4:7], v6, a6, a[4:7]
	s_nop 8
	v_readlane_b32 s52, v5, 3
	v_cndmask_b32_e64 v8, 0, v5, s[12:13]
	s_nop 0
	v_rcp_f32_e64 v9, -s52
	v_writelane_b32 v16, s52, 3
	v_mul_f32_e32 v7, v8, v9
	s_nop 1
	v_mfma_f32_16x16x4_f32 v[2:5], v7, v5, v[2:5]
	v_mfma_f32_16x16x4_f32 a[4:7], v7, a7, a[4:7]
	s_nop 8
	v_readlane_b32 s52, v2, 20
	v_cndmask_b32_e64 v8, 0, v2, s[14:15]
	s_nop 0
	v_rcp_f32_e64 v9, -s52
	v_writelane_b32 v16, s52, 4
	v_mul_f32_e32 v6, v8, v9
	s_nop 1
	v_mfma_f32_16x16x4_f32 v[2:5], v6, v2, v[2:5]
	v_mfma_f32_16x16x4_f32 a[4:7], v6, a4, a[4:7]
	s_nop 8
	v_readlane_b32 s52, v3, 21
	v_cndmask_b32_e64 v8, 0, v3, s[16:17]
	s_nop 0
	v_rcp_f32_e64 v9, -s52
	v_writelane_b32 v16, s52, 5
	v_mul_f32_e32 v7, v8, v9
	s_nop 1
	v_mfma_f32_16x16x4_f32 v[2:5], v7, v3, v[2:5]
	v_mfma_f32_16x16x4_f32 a[4:7], v7, a5, a[4:7]
	s_nop 8
	v_readlane_b32 s52, v4, 22
	v_cndmask_b32_e64 v8, 0, v4, s[18:19]
	s_nop 0
	v_rcp_f32_e64 v9, -s52
	v_writelane_b32 v16, s52, 6
	v_mul_f32_e32 v6, v8, v9
	s_nop 1
	v_mfma_f32_16x16x4_f32 v[2:5], v6, v4, v[2:5]
	v_mfma_f32_16x16x4_f32 a[4:7], v6, a6, a[4:7]
	s_nop 8
	v_readlane_b32 s52, v5, 23
	v_cndmask_b32_e64 v8, 0, v5, s[20:21]
	s_nop 0
	v_rcp_f32_e64 v9, -s52
	v_writelane_b32 v16, s52, 7
	v_mul_f32_e32 v7, v8, v9
	s_nop 1
	v_mfma_f32_16x16x4_f32 v[2:5], v7, v5, v[2:5]
	v_mfma_f32_16x16x4_f32 a[4:7], v7, a7, a[4:7]
	s_nop 8
	v_readlane_b32 s52, v2, 40
	v_cndmask_b32_e64 v8, 0, v2, s[22:23]
	s_nop 0
	v_rcp_f32_e64 v9, -s52
	v_writelane_b32 v16, s52, 8
	v_mul_f32_e32 v6, v8, v9
	s_nop 1
	v_mfma_f32_16x16x4_f32 v[2:5], v6, v2, v[2:5]
	v_mfma_f32_16x16x4_f32 a[4:7], v6, a4, a[4:7]
	s_nop 8
	v_readlane_b32 s52, v3, 41
	v_cndmask_b32_e64 v8, 0, v3, s[24:25]
	s_nop 0
	v_rcp_f32_e64 v9, -s52
	v_writelane_b32 v16, s52, 9
	v_mul_f32_e32 v7, v8, v9
	s_nop 1
	v_mfma_f32_16x16x4_f32 v[2:5], v7, v3, v[2:5]
	v_mfma_f32_16x16x4_f32 a[4:7], v7, a5, a[4:7]
	s_nop 8
	v_readlane_b32 s52, v4, 42
	v_cndmask_b32_e64 v8, 0, v4, s[26:27]
	s_nop 0
	v_rcp_f32_e64 v9, -s52
	v_writelane_b32 v16, s52, 10
	v_mul_f32_e32 v6, v8, v9
	s_nop 1
	v_mfma_f32_16x16x4_f32 v[2:5], v6, v4, v[2:5]
	v_mfma_f32_16x16x4_f32 a[4:7], v6, a6, a[4:7]
	s_nop 8
	v_readlane_b32 s52, v5, 43
	v_cndmask_b32_e64 v8, 0, v5, s[28:29]
	s_nop 0
	v_rcp_f32_e64 v9, -s52
	v_writelane_b32 v16, s52, 11
	v_mul_f32_e32 v7, v8, v9
	s_nop 1
	v_mfma_f32_16x16x4_f32 v[2:5], v7, v5, v[2:5]
	v_mfma_f32_16x16x4_f32 a[4:7], v7, a7, a[4:7]
	s_nop 8
	v_readlane_b32 s52, v2, 60
	v_cndmask_b32_e64 v8, 0, v2, s[30:31]
	s_nop 0
	v_rcp_f32_e64 v9, -s52
	v_writelane_b32 v16, s52, 12
	v_mul_f32_e32 v6, v8, v9
	s_nop 1
	v_mfma_f32_16x16x4_f32 v[2:5], v6, v2, v[2:5]
	v_mfma_f32_16x16x4_f32 a[4:7], v6, a4, a[4:7]
	s_nop 8
	v_readlane_b32 s52, v3, 61
	v_cndmask_b32_e64 v8, 0, v3, s[34:35]
	s_nop 0
	v_rcp_f32_e64 v9, -s52
	v_writelane_b32 v16, s52, 13
	v_mul_f32_e32 v7, v8, v9
	s_nop 1
	v_mfma_f32_16x16x4_f32 v[2:5], v7, v3, v[2:5]
	v_mfma_f32_16x16x4_f32 a[4:7], v7, a5, a[4:7]
	s_nop 8
	v_readlane_b32 s52, v4, 62
	v_cndmask_b32_e64 v8, 0, v4, s[36:37]
	s_nop 0
	v_rcp_f32_e64 v9, -s52
	v_writelane_b32 v16, s52, 14
	v_mul_f32_e32 v6, v8, v9
	s_nop 1
	v_mfma_f32_16x16x4_f32 v[2:5], v6, v4, v[2:5]
	v_mfma_f32_16x16x4_f32 a[4:7], v6, a6, a[4:7]
	s_nop 8
	v_readlane_b32 s52, v5, 63
	s_nop 1
	v_writelane_b32 v16, s52, 15
	v_accvgpr_read_b32 v9, a7
	v_accvgpr_read_b32 v8, a6
	v_accvgpr_read_b32 v7, a5
	v_accvgpr_read_b32 v6, a4
	s_and_saveexec_b64 s[52:53], s[4:5]
	s_cbranch_execz .LBB1_234
	s_waitcnt lgkmcnt(2)
	v_lshl_add_u32 v17, s97, 2, v134
	ds_write_b32 v17, v16

.Lp1_go_3:
	v_accvgpr_write_b32 a4, v22
	v_accvgpr_write_b32 a5, v23
	v_accvgpr_write_b32 a6, v24
	v_readlane_b32 s52, v2, 0
	v_accvgpr_write_b32 a7, v25
	v_cmp_lt_i32_e32 vcc, 0, v21
	v_rcp_f32_e64 v9, -s52
	v_writelane_b32 v53, s52, 0
	v_cndmask_b32_e64 v8, 0, v2, s[4:5]
	v_mul_f32_e32 v6, v8, v9
	s_nop 1
	v_mfma_f32_16x16x4_f32 v[2:5], v6, v2, v[2:5]
	v_mfma_f32_16x16x4_f32 a[4:7], v6, v22, a[4:7]
	s_nop 8
	v_readlane_b32 s52, v3, 1
	v_cndmask_b32_e64 v8, 0, v3, s[6:7]
	s_nop 0
	v_rcp_f32_e64 v9, -s52
	v_writelane_b32 v53, s52, 1
	v_mul_f32_e32 v7, v8, v9
	s_nop 1
	v_mfma_f32_16x16x4_f32 v[2:5], v7, v3, v[2:5]
	v_mfma_f32_16x16x4_f32 a[4:7], v7, a5, a[4:7]
	s_nop 8
	v_readlane_b32 s52, v4, 2
	v_cndmask_b32_e64 v8, 0, v4, s[8:9]
	s_nop 0
	v_rcp_f32_e64 v9, -s52
	v_writelane_b32 v53, s52, 2
	v_mul_f32_e32 v6, v8, v9
	s_nop 1
	v_mfma_f32_16x16x4_f32 v[2:5], v6, v4, v[2:5]
	v_mfma_f32_16x16x4_f32 a[4:7], v6, a6, a[4:7]
	s_nop 8
	v_readlane_b32 s52, v5, 3
	v_cndmask_b32_e64 v8, 0, v5, s[10:11]
	s_nop 0
	v_rcp_f32_e64 v9, -s52
	v_writelane_b32 v53, s52, 3
	v_mul_f32_e32 v7, v8, v9
	s_nop 1
	v_mfma_f32_16x16x4_f32 v[2:5], v7, v5, v[2:5]
	v_mfma_f32_16x16x4_f32 a[4:7], v7, a7, a[4:7]
	s_nop 8
	v_readlane_b32 s52, v2, 20
	v_cndmask_b32_e64 v8, 0, v2, s[12:13]
	s_nop 0
	v_rcp_f32_e64 v9, -s52
	v_writelane_b32 v53, s52, 4
	v_mul_f32_e32 v6, v8, v9
	s_nop 1
	v_mfma_f32_16x16x4_f32 v[2:5], v6, v2, v[2:5]
	v_mfma_f32_16x16x4_f32 a[4:7], v6, a4, a[4:7]
	s_nop 8
	v_readlane_b32 s52, v3, 21
	v_cndmask_b32_e64 v8, 0, v3, s[14:15]
	s_nop 0
	v_rcp_f32_e64 v9, -s52
	v_writelane_b32 v53, s52, 5
	v_mul_f32_e32 v7, v8, v9
	s_nop 1
	v_mfma_f32_16x16x4_f32 v[2:5], v7, v3, v[2:5]
	v_mfma_f32_16x16x4_f32 a[4:7], v7, a5, a[4:7]
	s_nop 8
	v_readlane_b32 s52, v4, 22
	v_cndmask_b32_e64 v8, 0, v4, s[16:17]
	s_nop 0
	v_rcp_f32_e64 v9, -s52
	v_writelane_b32 v53, s52, 6
	v_mul_f32_e32 v6, v8, v9
	s_nop 1
	v_mfma_f32_16x16x4_f32 v[2:5], v6, v4, v[2:5]
	v_mfma_f32_16x16x4_f32 a[4:7], v6, a6, a[4:7]
	s_nop 8
	v_readlane_b32 s52, v5, 23
	v_cndmask_b32_e64 v8, 0, v5, s[18:19]
	s_nop 0
	v_rcp_f32_e64 v9, -s52
	v_writelane_b32 v53, s52, 7
	v_mul_f32_e32 v7, v8, v9
	s_nop 1
	v_mfma_f32_16x16x4_f32 v[2:5], v7, v5, v[2:5]
	v_mfma_f32_16x16x4_f32 a[4:7], v7, a7, a[4:7]
	s_nop 8
	v_readlane_b32 s52, v2, 40
	v_cndmask_b32_e64 v8, 0, v2, s[20:21]
	s_nop 0
	v_rcp_f32_e64 v9, -s52
	v_writelane_b32 v53, s52, 8
	v_mul_f32_e32 v6, v8, v9
	s_nop 1
	v_mfma_f32_16x16x4_f32 v[2:5], v6, v2, v[2:5]
	v_mfma_f32_16x16x4_f32 a[4:7], v6, a4, a[4:7]
	s_nop 8
	v_readlane_b32 s52, v3, 41
	v_cndmask_b32_e64 v8, 0, v3, s[22:23]
	s_nop 0
	v_rcp_f32_e64 v9, -s52
	v_writelane_b32 v53, s52, 9
	v_mul_f32_e32 v7, v8, v9
	s_nop 1
	v_mfma_f32_16x16x4_f32 v[2:5], v7, v3, v[2:5]
	v_mfma_f32_16x16x4_f32 a[4:7], v7, a5, a[4:7]
	s_nop 8
	v_readlane_b32 s52, v4, 42
	v_cndmask_b32_e64 v8, 0, v4, s[24:25]
	s_nop 0
	v_rcp_f32_e64 v9, -s52
	v_writelane_b32 v53, s52, 10
	v_mul_f32_e32 v6, v8, v9
	s_nop 1
	v_mfma_f32_16x16x4_f32 v[2:5], v6, v4, v[2:5]
	v_mfma_f32_16x16x4_f32 a[4:7], v6, a6, a[4:7]
	s_nop 8
	v_readlane_b32 s52, v5, 43
	v_cndmask_b32_e64 v8, 0, v5, s[26:27]
	s_nop 0
	v_rcp_f32_e64 v9, -s52
	v_writelane_b32 v53, s52, 11
	v_mul_f32_e32 v7, v8, v9
	s_nop 1
	v_mfma_f32_16x16x4_f32 v[2:5], v7, v5, v[2:5]
	v_mfma_f32_16x16x4_f32 a[4:7], v7, a7, a[4:7]
	s_nop 8
	v_readlane_b32 s52, v2, 60
	v_cndmask_b32_e64 v8, 0, v2, s[28:29]
	s_nop 0
	v_rcp_f32_e64 v9, -s52
	v_writelane_b32 v53, s52, 12
	v_mul_f32_e32 v6, v8, v9
	s_nop 1
	v_mfma_f32_16x16x4_f32 v[2:5], v6, v2, v[2:5]
	v_mfma_f32_16x16x4_f32 a[4:7], v6, a4, a[4:7]
	s_nop 8
	v_readlane_b32 s52, v3, 61
	v_cndmask_b32_e64 v8, 0, v3, s[30:31]
	s_nop 0
	v_rcp_f32_e64 v9, -s52
	v_writelane_b32 v53, s52, 13
	v_mul_f32_e32 v7, v8, v9
	s_nop 1
	v_mfma_f32_16x16x4_f32 v[2:5], v7, v3, v[2:5]
	v_mfma_f32_16x16x4_f32 a[4:7], v7, a5, a[4:7]
	s_nop 8
	v_readlane_b32 s52, v4, 62
	v_cndmask_b32_e64 v8, 0, v4, s[34:35]
	s_nop 0
	v_rcp_f32_e64 v9, -s52
	v_writelane_b32 v53, s52, 14
	v_mul_f32_e32 v6, v8, v9
	s_nop 1
	v_mfma_f32_16x16x4_f32 v[2:5], v6, v4, v[2:5]
	v_mfma_f32_16x16x4_f32 a[4:7], v6, a6, a[4:7]
	s_nop 8
	v_readlane_b32 s52, v5, 63
	s_nop 1
	v_writelane_b32 v53, s52, 15
	v_accvgpr_read_b32 v9, a7
	v_accvgpr_read_b32 v8, a6
	v_accvgpr_read_b32 v7, a5
	v_accvgpr_read_b32 v6, a4
	s_and_saveexec_b64 s[52:53], s[2:3]
	s_cbranch_execz .LBB1_304
	s_waitcnt lgkmcnt(2)
	v_lshl_add_u32 v54, s80, 2, v11
	ds_write_b32 v54, v53

.Lp1_go_4:
	v_accvgpr_write_b32 a4, v22
	v_accvgpr_write_b32 a5, v23
	v_accvgpr_write_b32 a6, v24
	v_readlane_b32 s52, v0, 0
	v_accvgpr_write_b32 a7, v25
	v_cmp_lt_i32_e32 vcc, 0, v21
	v_rcp_f32_e64 v7, -s52
	v_writelane_b32 v36, s52, 0
	v_cndmask_b32_e64 v6, 0, v0, s[4:5]
	v_mul_f32_e32 v4, v6, v7
	s_nop 1
	v_mfma_f32_16x16x4_f32 v[0:3], v4, v0, v[0:3]
	v_mfma_f32_16x16x4_f32 a[4:7], v4, v22, a[4:7]
	s_nop 8
	v_readlane_b32 s52, v1, 1
	v_cndmask_b32_e64 v6, 0, v1, s[6:7]
	s_nop 0
	v_rcp_f32_e64 v7, -s52
	v_writelane_b32 v36, s52, 1
	v_mul_f32_e32 v5, v6, v7
	s_nop 1
	v_mfma_f32_16x16x4_f32 v[0:3], v5, v1, v[0:3]
	v_mfma_f32_16x16x4_f32 a[4:7], v5, a5, a[4:7]
	s_nop 8
	v_readlane_b32 s52, v2, 2
	v_cndmask_b32_e64 v6, 0, v2, s[8:9]
	s_nop 0
	v_rcp_f32_e64 v7, -s52
	v_writelane_b32 v36, s52, 2
	v_mul_f32_e32 v4, v6, v7
	s_nop 1
	v_mfma_f32_16x16x4_f32 v[0:3], v4, v2, v[0:3]
	v_mfma_f32_16x16x4_f32 a[4:7], v4, a6, a[4:7]
	s_nop 8
	v_readlane_b32 s52, v3, 3
	v_cndmask_b32_e64 v6, 0, v3, s[10:11]
	s_nop 0
	v_rcp_f32_e64 v7, -s52
	v_writelane_b32 v36, s52, 3
	v_mul_f32_e32 v5, v6, v7
	s_nop 1
	v_mfma_f32_16x16x4_f32 v[0:3], v5, v3, v[0:3]
	v_mfma_f32_16x16x4_f32 a[4:7], v5, a7, a[4:7]
	s_nop 8
	v_readlane_b32 s52, v0, 20
	v_cndmask_b32_e64 v6, 0, v0, s[12:13]
	s_nop 0
	v_rcp_f32_e64 v7, -s52
	v_writelane_b32 v36, s52, 4
	v_mul_f32_e32 v4, v6, v7
	s_nop 1
	v_mfma_f32_16x16x4_f32 v[0:3], v4, v0, v[0:3]
	v_mfma_f32_16x16x4_f32 a[4:7], v4, a4, a[4:7]
	s_nop 8
	v_readlane_b32 s52, v1, 21
	v_cndmask_b32_e64 v6, 0, v1, s[14:15]
	s_nop 0
	v_rcp_f32_e64 v7, -s52
	v_writelane_b32 v36, s52, 5
	v_mul_f32_e32 v5, v6, v7
	s_nop 1
	v_mfma_f32_16x16x4_f32 v[0:3], v5, v1, v[0:3]
	v_mfma_f32_16x16x4_f32 a[4:7], v5, a5, a[4:7]
	s_nop 8
	v_readlane_b32 s52, v2, 22
	v_cndmask_b32_e64 v6, 0, v2, s[16:17]
	s_nop 0
	v_rcp_f32_e64 v7, -s52
	v_writelane_b32 v36, s52, 6
	v_mul_f32_e32 v4, v6, v7
	s_nop 1
	v_mfma_f32_16x16x4_f32 v[0:3], v4, v2, v[0:3]
	v_mfma_f32_16x16x4_f32 a[4:7], v4, a6, a[4:7]
	s_nop 8
	v_readlane_b32 s52, v3, 23
	v_cndmask_b32_e64 v6, 0, v3, s[18:19]
	s_nop 0
	v_rcp_f32_e64 v7, -s52
	v_writelane_b32 v36, s52, 7
	v_mul_f32_e32 v5, v6, v7
	s_nop 1
	v_mfma_f32_16x16x4_f32 v[0:3], v5, v3, v[0:3]
	v_mfma_f32_16x16x4_f32 a[4:7], v5, a7, a[4:7]
	s_nop 8
	v_readlane_b32 s52, v0, 40
	v_cndmask_b32_e64 v6, 0, v0, s[20:21]
	s_nop 0
	v_rcp_f32_e64 v7, -s52
	v_writelane_b32 v36, s52, 8
	v_mul_f32_e32 v4, v6, v7
	s_nop 1
	v_mfma_f32_16x16x4_f32 v[0:3], v4, v0, v[0:3]
	v_mfma_f32_16x16x4_f32 a[4:7], v4, a4, a[4:7]
	s_nop 8
	v_readlane_b32 s52, v1, 41
	v_cndmask_b32_e64 v6, 0, v1, s[22:23]
	s_nop 0
	v_rcp_f32_e64 v7, -s52
	v_writelane_b32 v36, s52, 9
	v_mul_f32_e32 v5, v6, v7
	s_nop 1
	v_mfma_f32_16x16x4_f32 v[0:3], v5, v1, v[0:3]
	v_mfma_f32_16x16x4_f32 a[4:7], v5, a5, a[4:7]
	s_nop 8
	v_readlane_b32 s52, v2, 42
	v_cndmask_b32_e64 v6, 0, v2, s[24:25]
	s_nop 0
	v_rcp_f32_e64 v7, -s52
	v_writelane_b32 v36, s52, 10
	v_mul_f32_e32 v4, v6, v7
	s_nop 1
	v_mfma_f32_16x16x4_f32 v[0:3], v4, v2, v[0:3]
	v_mfma_f32_16x16x4_f32 a[4:7], v4, a6, a[4:7]
	s_nop 8
	v_readlane_b32 s52, v3, 43
	v_cndmask_b32_e64 v6, 0, v3, s[26:27]
	s_nop 0
	v_rcp_f32_e64 v7, -s52
	v_writelane_b32 v36, s52, 11
	v_mul_f32_e32 v5, v6, v7
	s_nop 1
	v_mfma_f32_16x16x4_f32 v[0:3], v5, v3, v[0:3]
	v_mfma_f32_16x16x4_f32 a[4:7], v5, a7, a[4:7]
	s_nop 8
	v_readlane_b32 s52, v0, 60
	v_cndmask_b32_e64 v6, 0, v0, s[28:29]
	s_nop 0
	v_rcp_f32_e64 v7, -s52
	v_writelane_b32 v36, s52, 12
	v_mul_f32_e32 v4, v6, v7
	s_nop 1
	v_mfma_f32_16x16x4_f32 v[0:3], v4, v0, v[0:3]
	v_mfma_f32_16x16x4_f32 a[4:7], v4, a4, a[4:7]
	s_nop 8
	v_readlane_b32 s52, v1, 61
	v_cndmask_b32_e64 v6, 0, v1, s[30:31]
	s_nop 0
	v_rcp_f32_e64 v7, -s52
	v_writelane_b32 v36, s52, 13
	v_mul_f32_e32 v5, v6, v7
	s_nop 1
	v_mfma_f32_16x16x4_f32 v[0:3], v5, v1, v[0:3]
	v_mfma_f32_16x16x4_f32 a[4:7], v5, a5, a[4:7]
	s_nop 8
	v_readlane_b32 s52, v2, 62
	v_cndmask_b32_e64 v6, 0, v2, s[34:35]
	s_nop 0
	v_rcp_f32_e64 v7, -s52
	v_writelane_b32 v36, s52, 14
	v_mul_f32_e32 v4, v6, v7
	s_nop 1
	v_mfma_f32_16x16x4_f32 v[0:3], v4, v2, v[0:3]
	v_mfma_f32_16x16x4_f32 a[4:7], v4, a6, a[4:7]
	s_nop 8
	v_readlane_b32 s52, v3, 63
	s_nop 1
	v_writelane_b32 v36, s52, 15
	v_accvgpr_read_b32 v7, a7
	v_accvgpr_read_b32 v6, a6
	v_accvgpr_read_b32 v5, a5
	v_accvgpr_read_b32 v4, a4
	s_and_saveexec_b64 s[52:53], s[2:3]
	s_cbranch_execz .LBB1_345
	s_waitcnt lgkmcnt(2)
	v_lshl_add_u32 v37, s75, 2, v11
	ds_write_b32 v37, v36
